# allsys_1
# baseline (speedup 1.0000x reference)
.LBB0_4:
	s_or_b64 exec, exec, s[2:3]
	v_mov_b32_e32 v1, 0
	s_waitcnt lgkmcnt(0)
	s_barrier
	ds_read2_b32 v[32:33], v1 offset0:3 offset1:7
	ds_read2_b32 v[34:35], v1 offset0:1 offset1:2
	ds_read2_b32 v[36:37], v1 offset0:5 offset1:6
	s_movk_i32 s6, 0xc0
	v_cmp_gt_u32_e32 vcc, s6, v0
	s_movk_i32 s6, 0x80
	s_waitcnt lgkmcnt(2)
	v_fmac_f32_e32 v33, 0, v32
	v_cndmask_b32_e32 v1, 0, v33, vcc
	s_waitcnt lgkmcnt(0)
	v_fma_f32 v32, v35, v1, v37
	v_cmp_gt_u32_e32 vcc, s6, v0
	s_load_dwordx4 s[0:3], s[0:1], 0x30
	s_nop 0
	v_cndmask_b32_e32 v1, v1, v32, vcc
	v_fmac_f32_e32 v36, v34, v1
	v_cmp_gt_u32_e32 vcc, 64, v0
	s_nop 1
	v_cndmask_b32_e32 v0, v1, v36, vcc
	v_mov_b32_e32 v1, s5
	v_fmac_f32_e32 v1, s4, v0
	v_fmac_f32_e32 v24, v28, v1
	v_fmac_f32_e32 v30, v31, v0
	s_nop 0
	v_mov_b32_dpp v1, v24 wave_shl:1 row_mask:0xf bank_mask:0xf
	v_fmac_f32_e32 v13, v23, v1
	v_mov_b32_dpp v0, v30 wave_shl:1 row_mask:0xf bank_mask:0xf
	v_fmac_f32_e32 v12, v22, v13
	v_fmac_f32_e32 v17, v29, v0
	v_fmac_f32_e32 v11, v21, v12
	v_fmac_f32_e32 v16, v27, v17
	v_fmac_f32_e32 v10, v20, v11
	s_waitcnt lgkmcnt(0)
	v_lshl_add_u64 v[20:21], s[0:1], 0, v[18:19]
	v_fmac_f32_e32 v15, v26, v16
	v_pk_add_f32 v[4:5], v[12:13], v[4:5]
	v_pk_add_f32 v[2:3], v[10:11], v[2:3]
	global_store_dwordx4 v[20:21], v[10:13], off sc0 sc1 nt
	v_fmac_f32_e32 v14, v25, v15
	v_pk_add_f32 v[0:1], v[14:15], v[6:7]
	v_lshl_add_u64 v[10:11], s[2:3], 0, v[18:19]
	global_store_dwordx4 v[10:11], v[2:5], off sc0 sc1 nt
	s_nop 1
	v_pk_add_f32 v[2:3], v[16:17], v[8:9]
	global_store_dwordx4 v[20:21], v[14:17], off offset:1024 sc0 sc1 nt
	global_store_dwordx4 v[10:11], v[0:3], off offset:1024 sc0 sc1 nt
	s_endpgm
